# GEMM phases: one static s_setprio 1 for the trailing wave half (waves 4-7) at phase entry, toggles removed
# baseline (speedup 1.0000x reference)
; #define PG8_STAGE(bufoff, gbase, voff) do { _Pragma("unroll") for (int _i = 0; _i < 2; ++_i) \
;         __builtin_amdgcn_global_load_lds((const unsigned*)((const char*)(gbase) + (voff)[_i]), (PG8_LAS unsigned*)(lds + (bufoff) + ldsw + _i * 8192), 16, 0, 0); } while (0)
; #define PG8_WAIT_V(n) asm volatile("s_waitcnt vmcnt(" #n ")" ::: "memory")
; #define PG8_BAR __builtin_amdgcn_s_barrier()
; template <class Epi, class Sched, bool ALIGN_EPI = false, bool SP2 = false>
; __device__ __forceinline__ void gemm_phase(PG8_LAS unsigned char* lds, const Gemm g, const Sched& S, const Epi& E) {
;     ...
;     if constexpr (SP2) {
;         PG8_STAGE(PG8_SB(0, 0), cB, voffB); PG8_STAGE(PG8_SB(0, 1), cB + hstep, voffB); PG8_STAGE(PG8_SA(0, 0), cA, voffA); PG8_STAGE(PG8_SA(0, 1), cA + hstep, voffA);
;         if (wr == 1) PG8_BAR;
;         PG8_WAIT_V(2); PG8_BAR;
.LBB0_110:
	v_readfirstlane_b32 s98, v0
	s_setprio 0
	s_cmp_lt_u32 s98, 0x100
	s_cbranch_scc1 .Lprio_skip0
	s_setprio 1

; #define SEAM(k) do { if (IN(k) && IN((k) + 1)) xcd_barrier(bar); } while (0)
; #define REPS(k) for (bool again_ = true; again_; again_ = (((REP_MASK >> (k)) & 1) ? rep_again(MISC, bar) : false))
; __global__ void __launch_bounds__(NWAVES * 64, 2) hybrid_fwd(Params P) {
;     ...
;     SEAM(1);
;     if (IN(3)) REPS(3) {
;         if (bx < SCAN_WGS) gdn_scan(P, lds, bx, tid, lane, wave);
.LBB0_184:
	s_setprio 0
	v_readlane_b32 s4, v254, 2
	v_readlane_b32 s5, v254, 3
	s_cmp_lt_i32 s4, 4
	s_cselect_b64 s[0:1], -1, 0
	s_cmp_gt_i32 s5, 3
	v_writelane_b32 v255, s72, 2
	s_cselect_b64 s[4:5], -1, 0
	s_and_b64 s[0:1], s[0:1], s[4:5]
	v_writelane_b32 v255, s73, 3
	v_writelane_b32 v255, s0, 4
	s_andn2_b64 vcc, exec, s[0:1]
	s_nop 0
	v_writelane_b32 v255, s1, 5
	s_cbranch_vccz .LBB0_185
	s_getpc_b64 s[98:99]

; #define LAS __attribute__((address_space(3)))
; #define LDS_WAIT() asm volatile("s_waitcnt lgkmcnt(0)" ::: "memory")
; #define REPS(k) for (bool again_ = true; again_; again_ = (((REP_MASK >> (k)) & 1) ? rep_again(MISC, bar) : false))
;     asm volatile("v_mbcnt_lo_u32_b32 %0, -1, 0\n\tv_mbcnt_hi_u32_b32 %0, -1, %0" : "=v"(lane));
;     {
;         LAS unsigned* lw0 = (LAS unsigned*)(lds) + wave * PE_WAVE_W + PE_NT * PE_TOK_W + PE_ENT_W;
;         peer_topk_wave(P, (LAS int*)lw0, lw0 + 32 * 33, (LAS float*)(lw0 + 32 * 33 + PE_NT * 128), tbase, lane);
;         LDS_WAIT(); asm volatile("" : "+v"(lane), "+s"(tbase) :: "memory");
;     }
;     const unsigned char* ws = P.ws;
;     const unsigned char* UB8 = ws + WS_UB; const unsigned char* VB8 = ws + WS_VB;
;     const float* USC = (const float*)(ws + WS_USC); const float* VSC = (const float*)(ws + WS_VSC);
;     f32x2 acc[PE_NT][8];
;     LAS unsigned* lw = (LAS unsigned*)(lds) + wave * PE_WAVE_W;
;     LAS unsigned* ents = lw + PE_NT * PE_TOK_W;
;     const unsigned voff = (unsigned)lane * 16u;
;     LAS unsigned* upe = ents + PE_ENT_W + 32 * 33; LAS float* upg = (LAS float*)(upe + PE_NT * 128);
;     LAS unsigned* hql = ents + PE_ENT_W;
; __global__ void __launch_bounds__(NWAVES * 64, 2) hybrid_fwd(Params P) {
;     ...
;     if (IN(11)) REPS(11) {
;     ...
;         for (int it = 0; it < 4; ++it) { const int tb = (bx * NWAVES + wave) * PE_NT + (it >> 1) * (G * NWAVES * PE_NT); if (tb < T) peer_pass(P, lds, tb, lane, wave, P.out, (it & 1) ? 0x3fff : PE_EXP_MASK); }
;     ...
;         for (int tb = (bx * NWAVES + wave) * PE_NT, np = 0; tb < T; tb += G * NWAVES * PE_NT, ++np) {
;             if (PE_PASS_BARRIER && np > 0 && (T % (G * NWAVES * PE_NT)) == 0) xcd_barrier(bar);
;             peer_pass(P, lds, tb, lane, wave, P.out);
.LBB0_2674:
	s_setprio 0
	s_cmp_lt_i32 s74, 12
	s_cselect_b64 s[0:1], -1, 0
	s_cmp_gt_i32 s75, 11
	s_cselect_b64 s[4:5], -1, 0
	s_and_b64 s[0:1], s[0:1], s[4:5]
	s_andn2_b64 vcc, exec, s[0:1]
	s_cbranch_vccnz .LBB0_2885
	s_lshl_b32 s0, s2, 5
	v_readlane_b32 s2, v254, 56
	s_lshl_b32 s1, s2, 2
	s_add_i32 s6, s1, s0
	s_cmpk_gt_i32 s6, 0x3fff
	v_readlane_b32 s3, v254, 57
	s_cbranch_scc1 .LBB0_2885
	v_readlane_b32 s0, v254, 56
	s_mulk_i32 s0, 0x4bc0
	s_add_i32 s90, s0, 0
	v_readlane_b32 s1, v254, 57
	s_add_u32 s0, s24, 0x7c00000
	s_addc_u32 s1, s25, 0
	s_add_u32 s70, s24, 0x6c00000
	v_writelane_b32 v255, s0, 7
	s_addc_u32 s71, s25, 0
	v_mov_b32_e32 v49, 0
	v_writelane_b32 v255, s1, 8
	s_add_u32 s0, s24, 0x1b40000
	s_addc_u32 s1, s25, 0
	v_writelane_b32 v254, s0, 4
	v_mbcnt_lo_u32_b32 v0, -1, 0
	s_mov_b32 s96, 0x80008000
	v_writelane_b32 v254, s1, 5
	s_add_u32 s0, s24, 0x1b60000
	s_addc_u32 s1, s25, 0
	v_writelane_b32 v254, s0, 2
	s_mov_b32 s97, 0xffff0000
	v_mov_b32_e32 v110, 0x358637bd
	v_writelane_b32 v254, s1, 3
	s_add_u32 s0, s24, 0x20000
	v_writelane_b32 v255, s0, 9
	s_addc_u32 s0, s25, 0
	s_add_u32 s82, s24, 0xe400000
	v_writelane_b32 v254, s0, 20
	s_addc_u32 s83, s25, 0
	s_add_i32 s0, s90, 0x1a70
	v_writelane_b32 v255, s0, 2
	s_lshl_b32 s0, s26, 5
	v_writelane_b32 v255, s0, 4
	s_add_i32 s0, s90, 0x1a40
	v_writelane_b32 v254, s0, 0
	v_mov_b32_e32 v111, 0x80
	v_mbcnt_hi_u32_b32 v112, -1, v0
	v_mov_b32_e32 v113, 0xc0135761
	s_mov_b32 s91, 0x5010400
	s_mov_b32 s92, 0x7030602
	s_mov_b32 s94, 0x5040100
	s_mov_b32 s68, 0x7060302
	v_mov_b32_e32 v114, 0x8000
	v_mov_b32_e32 v115, 0xffff
	v_mov_b32_e32 v116, 0xffffff00
	v_mov_b32_e32 v122, v49
	v_mov_b32_e32 v123, v49
	v_mov_b32_e32 v124, v49
	v_mov_b32_e32 v125, v49
	s_branch .LBB0_2679
